# karg80
# speedup vs baseline: 1.0335x; 1.0314x over previous
_Z11prep_kernelPKfS0_PKiS2_S0_S0_S0_S0_S0_S0_Pc:
	s_getpc_b64 s[36:37]
	s_add_u32 s36, s36, _Z11attn_kernelILi4EEvPKfS1_S1_S1_S1_S1_PKcPf@rel32@lo+4
	s_addc_u32 s37, s37, _Z11attn_kernelILi4EEvPKfS1_S1_S1_S1_S1_PKcPf@rel32@hi+12
	v_and_b32_e32 v192, 63, v0
	v_lshlrev_b32_e32 v192, 7, v192
	v_min_u32_e32 v192, 0x1180, v192
	global_load_dword v192, v192, s[36:37]
	s_lshr_b32 s4, s2, 2
	v_lshrrev_b32_e32 v2, 6, v0
	s_and_b32 s4, s4, 0x1ffffffe
	s_load_dwordx4 s[28:31], s[0:1], 0x40
	s_load_dwordx8 s[12:19], s[0:1], 0x0
	s_load_dwordx8 s[20:27], s[0:1], 0x20
	s_load_dwordx2 s[32:33], s[0:1], 0x50
	s_load_dword s40, s[0:1], 0x80
	v_and_b32_e32 v1, 15, v0
	s_and_b32 s3, s2, 7
	v_or_b32_e32 v2, s4, v2
	v_lshl_or_b32 v88, v2, 3, s3
	v_cmp_gt_u32_e64 s[10:11], 14, v1
	v_mul_lo_u32 v7, v88, 14
	v_and_b32_e32 v105, 63, v0
	v_cndmask_b32_e64 v6, 13, v1, s[10:11]
	v_add_u32_e32 v2, v7, v6
	v_mul_u32_u24_e32 v4, 12, v2
	v_lshlrev_b32_e32 v5, 2, v6
	v_cmp_gt_u32_e64 s[8:9], 48, v105
	v_cmp_gt_u32_e64 s[6:7], 14, v105
	v_lshlrev_b32_e32 v118, 1, v0
	v_lshrrev_b32_e32 v104, 4, v0
	v_cndmask_b32_e64 v8, 0, v105, s[8:9]
	v_cndmask_b32_e64 v9, 0, v105, s[6:7]
	v_mad_u32_u24 v8, v88, 48, v8
	v_add_lshl_u32 v9, v7, v9, 2
	v_lshlrev_b32_e32 v8, 2, v8
	s_lshl_b32 s2, s2, 3
	s_and_b32 s2, s2, 0x78
	v_and_b32_e32 v106, 30, v118
	v_or_b32_e32 v107, s2, v104
	v_cmp_gt_u32_e64 s[2:3], 23, v106
	v_or_b32_e32 v10, 1, v106
	v_cmp_gt_u32_e64 s[4:5], 23, v10
	v_lshlrev_b32_e32 v11, 7, v106
	v_lshlrev_b32_e32 v10, 7, v10
	v_cndmask_b32_e64 v11, 0, v11, s[2:3]
	v_cndmask_b32_e64 v10, 0, v10, s[4:5]
	v_or_b32_e32 v11, v11, v107
	v_or_b32_e32 v10, v10, v107
	v_lshlrev_b32_e32 v11, 2, v11
	v_lshlrev_b32_e32 v10, 2, v10
	v_lshlrev_b32_e32 v12, 2, v107
	v_lshlrev_b32_e32 v119, 5, v0
	v_lshlrev_b32_e32 v13, 2, v0
	v_and_b32_e32 v109, 12, v13
	v_and_b32_e32 v91, 0xf80, v119
	v_lshl_or_b32 v91, v109, 2, v91
	v_or_b32_e32 v92, 0x1000, v91
	v_lshlrev_b32_e32 v90, 9, v2
	v_and_b32_e32 v16, 48, v0
	v_or_b32_e32 v90, v90, v16
	v_or_b32_e32 v112, 0x80, v0
	v_or_b32_e32 v111, 0x180, v0
	v_or_b32_e32 v108, 0x280, v0
	v_mov_b32_e32 v87, 0
	v_bfe_u32 v110, v0, 4, 2
	s_movk_i32 s34, 0x60
	v_lshrrev_b32_e32 v136, 1, v0
	v_lshrrev_b32_e32 v18, 3, v0
	v_and_b32_e32 v18, 4, v18
	v_and_b32_e32 v19, 24, v0
	v_and_b32_e32 v20, 2, v136
	v_or3_b32 v18, v18, v19, v20
	v_and_or_b32 v136, v136, s34, v18
	v_mul_u32_u24_e32 v18, 0x110, v109
	v_lshl_add_u32 v136, v136, 1, v18
	v_add_u32_e32 v137, 0x1100, v136
	v_add_u32_e32 v138, 0x2200, v136
	v_lshlrev_b32_e32 v18, 9, v88
	v_and_b32_e32 v19, 0x100, v119
	v_lshlrev_b32_e32 v20, 4, v0
	v_and_b32_e32 v20, 48, v20
	v_or3_b32 v139, v18, v19, v20
	v_and_b32_e32 v19, 8, v118
	v_and_b32_e32 v20, 64, v118
	v_or3_b32 v139, v139, v19, v20
	v_lshlrev_b32_e32 v19, 2, v110
	v_and_b32_e32 v20, 4, v19
	v_or_b32_e32 v139, v139, v20
	v_lshl_or_b32 v140, v1, 5, v18
	v_or_b32_e32 v140, v140, v19
	v_add_u32_e32 v140, 0x80000, v140
	v_lshl_or_b32 v141, v88, 4, v1
	v_lshlrev_b32_e32 v141, 3, v141
	v_add_u32_e32 v141, 0x140000, v141
	v_lshlrev_b32_e32 v20, 8, v88
	v_mul_u32_u24_e32 v21, 43, v105
	v_lshrrev_b32_e32 v21, 9, v21
	v_mul_u32_u24_e32 v21, 12, v21
	v_sub_u32_e32 v22, v105, v21
	v_and_b32_e32 v142, 3, v22
	v_lshrrev_b32_e32 v22, 2, v22
	v_mad_u32_u24 v142, v142, 3, v22
	v_add_u32_e32 v142, v142, v21
	v_lshl_add_u32 v142, v142, 2, v20
	v_add_u32_e32 v142, 0x164000, v142
	v_lshl_add_u32 v143, v105, 2, v20
	v_add_u32_e32 v143, 0x164000, v143
	v_lshlrev_b32_e32 v123, 6, v107
	v_lshl_add_u32 v123, v106, 1, v123
	v_add_u32_e32 v123, 0x160000, v123
	v_lshl_add_u32 v122, v1, 4, v20
	v_or_b32_e32 v122, v122, v19
	v_add_u32_e32 v122, 0x100000, v122
	s_waitcnt lgkmcnt(0)
	global_load_dwordx3 v[82:84], v4, s[12:13]
	global_load_dword v85, v5, s[26:27]
	global_load_dword v114, v8, s[18:19]
	global_load_dword v115, v9, s[16:17]
	global_load_dword v116, v11, s[28:29]
	global_load_dword v113, v10, s[28:29]
	global_load_dword v117, v12, s[30:31]
	global_load_dwordx4 v[66:69], v91, s[20:21]
	global_load_dwordx4 v[70:73], v91, s[20:21] offset:64
	global_load_dwordx4 v[74:77], v92, s[20:21]
	global_load_dwordx4 v[78:81], v92, s[20:21] offset:64
	global_load_dwordx4 v[58:61], v91, s[22:23]
	global_load_dwordx4 v[62:65], v91, s[22:23] offset:64
	global_load_dwordx4 v[50:53], v92, s[22:23]
	global_load_dwordx4 v[54:57], v92, s[22:23] offset:64
	global_load_dwordx4 v[42:45], v91, s[24:25]
	global_load_dwordx4 v[46:49], v91, s[24:25] offset:64
	global_load_dwordx4 v[34:37], v92, s[24:25]
	global_load_dwordx4 v[38:41], v92, s[24:25] offset:64
	global_load_dwordx4 v[26:29], v90, s[14:15] nt
	global_load_dwordx4 v[30:33], v90, s[14:15] offset:64 nt
	global_load_dwordx4 v[18:21], v90, s[14:15] offset:128 nt
	global_load_dwordx4 v[22:25], v90, s[14:15] offset:192 nt
	global_load_dwordx4 v[10:13], v90, s[14:15] offset:256 nt
	global_load_dwordx4 v[14:17], v90, s[14:15] offset:320 nt
	global_load_dwordx4 v[2:5], v90, s[14:15] offset:384 nt
	global_load_dwordx4 v[6:9], v90, s[14:15] offset:448 nt
	s_waitcnt vmcnt(26)
	v_mov_b32_e32 v90, v83
	v_mov_b32_e32 v91, v84
	v_lshlrev_b32_e32 v86, 2, v110
	s_waitcnt vmcnt(25)
	v_mul_f32_e32 v84, 0x3fb8aa3b, v85
	s_mov_b32 s14, 0x41700000
	v_exp_f32_e32 v84, v84
	v_cndmask_b32_e64 v94, 0, 1.0, s[10:11]
	v_add_f32_e32 v84, 1.0, v84
	v_cmp_lt_f32_e32 vcc, s14, v85
	v_log_f32_e32 v84, v84
	v_cmp_lt_u32_e64 s[12:13], 15, v105
	v_mul_f32_e32 v84, 0x3f317218, v84
	v_cndmask_b32_e32 v84, v84, v85, vcc
	v_mul_f32_e32 v84, 0xbe715bef, v84
	v_mul_f32_e32 v84, 0x3f3504f3, v84
	v_mul_f32_e32 v84, 0x41800000, v84
	v_cndmask_b32_e64 v99, 0, v84, s[10:11]
	v_mul_f32_e32 v101, -2.0, v99
	v_mul_f32_e32 v100, v82, v82
	v_cmp_gt_u32_e32 vcc, 16, v105
	v_fmac_f32_e32 v100, v90, v90
	v_cmp_eq_u32_e64 s[12:13], 0, v110
	v_fmac_f32_e32 v100, v91, v91
	v_cmp_eq_u32_e64 s[14:15], 1, v110
	v_mul_f32_e32 v83, v101, v82
	v_cmp_eq_u32_e64 s[16:17], 2, v110
	v_mul_f32_e32 v84, v101, v90
	v_mul_f32_e32 v85, v101, v91
	v_mul_f32_e32 v89, v99, v100
	v_mul_f32_e32 v92, v82, v94
	v_mul_f32_e32 v93, v90, v94
	v_mul_f32_e32 v95, v91, v94
	v_mul_f32_e32 v96, v100, v94
	v_cvt_pk_fp8_f32 v88, v83, v83
	v_cvt_pk_fp8_f32 v104, v84, v84
	v_cvt_f32_fp8_e32 v97, v88
	v_cvt_f32_fp8_e32 v98, v104
	v_sub_f32_e32 v97, v83, v97
	v_sub_f32_e32 v98, v84, v98
	v_cvt_pk_fp8_f32 v88, v85, v85
	v_cvt_pk_fp8_f32 v104, v99, v99
	v_cvt_f32_fp8_e32 v101, v88
	v_cvt_f32_fp8_e32 v102, v104
	v_sub_f32_e32 v101, v85, v101
	v_sub_f32_e32 v102, v99, v102
	v_cvt_pk_fp8_f32 v88, v89, v89
	v_cvt_pk_fp8_f32 v104, v92, v92
	v_cvt_f32_fp8_e32 v103, v88
	v_cvt_f32_fp8_e32 v120, v104
	v_sub_f32_e32 v103, v89, v103
	v_sub_f32_e32 v120, v92, v120
	v_cvt_pk_fp8_f32 v88, v93, v93
	v_cvt_pk_fp8_f32 v104, v95, v95
	v_cvt_f32_fp8_e32 v121, v88
	v_cvt_f32_fp8_e32 v86, v104
	v_sub_f32_e32 v121, v93, v121
	v_sub_f32_e32 v86, v95, v86
	v_cvt_pk_fp8_f32 v88, v96, v96
	s_nop 0
	v_cvt_f32_fp8_e32 v87, v88
	s_nop 0
	v_sub_f32_e32 v87, v96, v87
	v_cndmask_b32_e64 v124, v89, v85, s[16:17]
	v_cndmask_b32_e64 v124, v124, v98, s[14:15]
	v_cndmask_b32_e64 v124, v124, v83, s[12:13]
	v_cndmask_b32_e64 v125, v103, v99, s[16:17]
	v_cndmask_b32_e64 v125, v125, v84, s[14:15]
	v_cndmask_b32_e64 v125, v125, v97, s[12:13]
	v_cndmask_b32_e64 v126, 0, v102, s[16:17]
	v_cndmask_b32_e64 v126, v126, v85, s[14:15]
	v_cndmask_b32_e64 v126, v126, v83, s[12:13]
	v_cndmask_b32_e64 v127, 0, v99, s[16:17]
	v_cndmask_b32_e64 v127, v127, v101, s[14:15]
	v_cndmask_b32_e64 v127, v127, v84, s[12:13]
	v_cndmask_b32_e64 v128, v94, v86, s[16:17]
	v_cndmask_b32_e64 v128, v128, v93, s[14:15]
	v_cndmask_b32_e64 v128, v128, v92, s[12:13]
	v_cndmask_b32_e64 v129, v94, v96, s[16:17]
	v_cndmask_b32_e64 v129, v129, v121, s[14:15]
	v_cndmask_b32_e64 v129, v129, v92, s[12:13]
	v_cndmask_b32_e64 v130, 0, v96, s[16:17]
	v_cndmask_b32_e64 v130, v130, v95, s[14:15]
	v_cndmask_b32_e64 v130, v130, v120, s[12:13]
	v_cndmask_b32_e64 v131, 0, v87, s[16:17]
	v_cndmask_b32_e64 v131, v131, v95, s[14:15]
	v_cndmask_b32_e64 v131, v131, v93, s[12:13]
	v_cvt_pk_fp8_f32 v119, v124, v125
	v_cvt_pk_fp8_f32 v103, v128, v129
	v_cvt_pk_fp8_f32 v119, v126, v127 op_sel:[0,0,1]
	v_cvt_pk_fp8_f32 v103, v130, v131 op_sel:[0,0,1]
	s_nop 0
	global_store_dword v139, v119, s[32:33] offset:128
	global_store_dword v140, v103, s[32:33] offset:16
	s_and_saveexec_b64 s[0:1], vcc
	s_cbranch_execz .LBB0_14
	v_cvt_f16_f32_e32 v83, v82
	v_cvt_pk_f16_f32 v90, v90, v91
	s_nop 0
	v_alignbit_b32 v91, 0, v90, 16
	v_pack_b32_f16 v90, v83, v90
	global_store_dwordx2 v141, v[90:91], s[32:33]
